# v75 with MoE GEMM2 tail conversion sites starting at vcu 128 instead of 144 (4224 items hidden)
# baseline (speedup 1.0000x reference)
.LBB0_55:
	s_cmp_lg_u32 s99, 0
	s_cbranch_scc1 .Ltc_itemdone
	v_readlane_b32 s2, v254, 0
	v_readlane_b32 s3, v254, 1
	s_load_dword s0, s[2:3], 0xe8
	s_add_i32 s14, s14, s15
	s_add_i32 s16, s16, s17
	s_add_i32 s10, s10, s18
	s_waitcnt lgkmcnt(0)
	s_add_i32 s22, s22, s0
	s_cmp_lt_i32 s22, 0x1380
	s_cbranch_scc1 .Ltc_noskip
	s_cmp_ge_i32 s22, 0x2000
	s_cbranch_scc1 .Ltc_noskip
	s_and_b32 s22, s22, 0xff
	s_addk_i32 s22, 0x2000
	s_lshl_b32 s14, s22, 5
	s_lshl_b32 s16, s22, 4
	s_lshl_b32 s10, s22, 9

.Ltc_next:
	s_cmp_ge_u32 s100, 0x1080
	s_cbranch_scc1 .Ltc_alldone
	s_movk_i32 s0, 0x1f80
	s_cmp_lt_u32 s100, 0xc80
	s_cselect_b32 s22, 0x1380, s0
	s_add_i32 s22, s22, s100
	v_mbcnt_lo_u32_b32 v0, -1, 0
	v_mbcnt_hi_u32_b32 v0, -1, v0
	s_and_b32 s0, s94, 0xffffffc0
	s_nop 0
	v_ashrrev_i32_e32 v1, 31, v0
	v_add_u32_e32 v2, s0, v0
	s_movk_i32 s0, 0x44
	v_lshlrev_b32_e32 v5, 7, v0
	v_mul_lo_u32 v4, v0, s0
	v_mul_lo_u32 v12, v2, s0
	v_lshrrev_b32_e32 v3, 1, v2
	v_and_b32_e32 v5, 0x80, v5
	s_movk_i32 s0, 0x7f
	v_and_or_b32 v3, v3, s0, v5
	s_lshl_b32 s6, s95, 3
	s_add_u32 s7, s88, 0x22000000
	s_addc_u32 s11, s89, 0
	v_add_u32_e32 v4, 0, v4
	s_add_u32 s12, s88, 0x2000000
	v_add_u32_e32 v4, s6, v4
	s_mov_b32 s1, 0
	s_addc_u32 s13, s89, 0
	s_lshl_b32 s14, s22, 5
	s_lshl_b32 s16, s22, 4
	s_lshl_b32 s10, s22, 9
	s_mov_b32 s19, 0xc3e00000
	s_movk_i32 s20, 0xff
	v_add_u32_e32 v5, 0x1100, v4
	v_add_u32_e32 v6, 0x2200, v4
	v_add_u32_e32 v7, 0x3300, v4
	v_add_u32_e32 v8, 0x4400, v4
	v_add_u32_e32 v9, 0x5500, v4
	v_add_u32_e32 v10, 0x6600, v4
	v_add_u32_e32 v11, 0x7700, v4
	v_add_u32_e32 v12, 0, v12
	s_movk_i32 s21, 0xff00
	v_mov_b32_e32 v13, 0x43e00000
	v_mov_b32_e32 v14, 8
	s_branch .LBB0_56

.LBB0_668:
	s_cmp_lt_u32 s96, 128
	s_cbranch_scc1 .Ltc_skip_4
	v_writelane_b32 v200, s0, 0
	s_nop 1
	v_writelane_b32 v200, s1, 1
	s_nop 1
	v_writelane_b32 v200, s2, 2
	s_nop 1
	v_writelane_b32 v200, s3, 3
	s_nop 1
	v_writelane_b32 v200, s4, 4
	s_nop 1
	v_writelane_b32 v200, s5, 5
	s_nop 1
	v_writelane_b32 v200, s6, 6
	s_nop 1
	v_writelane_b32 v200, s7, 7
	s_nop 1
	v_writelane_b32 v200, s10, 8
	s_nop 1
	v_writelane_b32 v200, s11, 9
	s_nop 1
	v_writelane_b32 v200, s12, 10
	s_nop 1
	v_writelane_b32 v200, s13, 11
	s_nop 1
	v_writelane_b32 v200, s14, 12
	s_nop 1
	v_writelane_b32 v200, s15, 13
	s_nop 1
	v_writelane_b32 v200, s16, 14
	s_nop 1
	v_writelane_b32 v200, s17, 15
	s_nop 1
	v_writelane_b32 v200, s18, 16
	s_nop 1
	v_writelane_b32 v200, s19, 17
	s_nop 1
	v_writelane_b32 v200, s20, 18
	s_nop 1
	v_writelane_b32 v200, s21, 19
	s_nop 1
	v_writelane_b32 v200, s22, 20
	s_nop 1
	v_writelane_b32 v200, s23, 21
	s_nop 1
	v_writelane_b32 v200, s24, 22
	s_nop 1
	v_writelane_b32 v200, s25, 23
	s_nop 1
	v_writelane_b32 v200, s36, 24
	s_nop 1
	v_writelane_b32 v200, s37, 25
	s_nop 1
	v_writelane_b32 v200, s38, 26
	s_nop 1
	v_writelane_b32 v200, s39, 27
	s_nop 1
	v_writelane_b32 v200, s40, 28
	s_nop 1
	v_writelane_b32 v200, s41, 29
	s_nop 1
	v_writelane_b32 v200, s42, 30
	s_nop 1
	v_writelane_b32 v200, s43, 31
	s_nop 1
	v_writelane_b32 v200, s44, 32
	s_nop 1
	v_writelane_b32 v200, s45, 33
	s_nop 1
	v_writelane_b32 v200, s46, 34
	s_nop 1
	v_writelane_b32 v200, s47, 35
	s_nop 1
	v_writelane_b32 v200, s48, 36
	s_nop 1
	v_writelane_b32 v200, s49, 37
	s_nop 1
	v_writelane_b32 v200, s50, 38
	s_nop 1
	v_writelane_b32 v200, s51, 39
	s_nop 1
	s_mov_b32 s99, 4
	s_mov_b32 s98, 2
	s_mov_b32 s101, 128
	s_add_i32 s100, s96, 960
	s_branch .Ltc_next

.LBB0_807:
	s_cmp_lt_u32 s96, 48
	s_cbranch_scc1 .Ltc_skip_5
	v_writelane_b32 v200, s0, 0
	s_nop 1
	v_writelane_b32 v200, s1, 1
	s_nop 1
	v_writelane_b32 v200, s2, 2
	s_nop 1
	v_writelane_b32 v200, s3, 3
	s_nop 1
	v_writelane_b32 v200, s4, 4
	s_nop 1
	v_writelane_b32 v200, s5, 5
	s_nop 1
	v_writelane_b32 v200, s6, 6
	s_nop 1
	v_writelane_b32 v200, s7, 7
	s_nop 1
	v_writelane_b32 v200, s10, 8
	s_nop 1
	v_writelane_b32 v200, s11, 9
	s_nop 1
	v_writelane_b32 v200, s12, 10
	s_nop 1
	v_writelane_b32 v200, s13, 11
	s_nop 1
	v_writelane_b32 v200, s14, 12
	s_nop 1
	v_writelane_b32 v200, s15, 13
	s_nop 1
	v_writelane_b32 v200, s16, 14
	s_nop 1
	v_writelane_b32 v200, s17, 15
	s_nop 1
	v_writelane_b32 v200, s18, 16
	s_nop 1
	v_writelane_b32 v200, s19, 17
	s_nop 1
	v_writelane_b32 v200, s20, 18
	s_nop 1
	v_writelane_b32 v200, s21, 19
	s_nop 1
	v_writelane_b32 v200, s22, 20
	s_nop 1
	v_writelane_b32 v200, s23, 21
	s_nop 1
	v_writelane_b32 v200, s24, 22
	s_nop 1
	v_writelane_b32 v200, s25, 23
	s_nop 1
	v_writelane_b32 v200, s36, 24
	s_nop 1
	v_writelane_b32 v200, s37, 25
	s_nop 1
	v_writelane_b32 v200, s38, 26
	s_nop 1
	v_writelane_b32 v200, s39, 27
	s_nop 1
	v_writelane_b32 v200, s40, 28
	s_nop 1
	v_writelane_b32 v200, s41, 29
	s_nop 1
	v_writelane_b32 v200, s42, 30
	s_nop 1
	v_writelane_b32 v200, s43, 31
	s_nop 1
	v_writelane_b32 v200, s44, 32
	s_nop 1
	v_writelane_b32 v200, s45, 33
	s_nop 1
	v_writelane_b32 v200, s46, 34
	s_nop 1
	v_writelane_b32 v200, s47, 35
	s_nop 1
	v_writelane_b32 v200, s48, 36
	s_nop 1
	v_writelane_b32 v200, s49, 37
	s_nop 1
	v_writelane_b32 v200, s50, 38
	s_nop 1
	v_writelane_b32 v200, s51, 39
	s_nop 1
	s_mov_b32 s99, 5
	s_mov_b32 s98, 2
	s_mov_b32 s101, 208
	s_add_i32 s100, s96, 1296
	s_branch .Ltc_next

.LBB0_1052:
	s_cmp_lt_u32 s96, 32
	s_cbranch_scc1 .Ltc_skip_6
	v_writelane_b32 v200, s0, 0
	s_nop 1
	v_writelane_b32 v200, s1, 1
	s_nop 1
	v_writelane_b32 v200, s2, 2
	s_nop 1
	v_writelane_b32 v200, s3, 3
	s_nop 1
	v_writelane_b32 v200, s4, 4
	s_nop 1
	v_writelane_b32 v200, s5, 5
	s_nop 1
	v_writelane_b32 v200, s6, 6
	s_nop 1
	v_writelane_b32 v200, s7, 7
	s_nop 1
	v_writelane_b32 v200, s10, 8
	s_nop 1
	v_writelane_b32 v200, s11, 9
	s_nop 1
	v_writelane_b32 v200, s12, 10
	s_nop 1
	v_writelane_b32 v200, s13, 11
	s_nop 1
	v_writelane_b32 v200, s14, 12
	s_nop 1
	v_writelane_b32 v200, s15, 13
	s_nop 1
	v_writelane_b32 v200, s16, 14
	s_nop 1
	v_writelane_b32 v200, s17, 15
	s_nop 1
	v_writelane_b32 v200, s18, 16
	s_nop 1
	v_writelane_b32 v200, s19, 17
	s_nop 1
	v_writelane_b32 v200, s20, 18
	s_nop 1
	v_writelane_b32 v200, s21, 19
	s_nop 1
	v_writelane_b32 v200, s22, 20
	s_nop 1
	v_writelane_b32 v200, s23, 21
	s_nop 1
	v_writelane_b32 v200, s24, 22
	s_nop 1
	v_writelane_b32 v200, s25, 23
	s_nop 1
	v_writelane_b32 v200, s36, 24
	s_nop 1
	v_writelane_b32 v200, s37, 25
	s_nop 1
	v_writelane_b32 v200, s38, 26
	s_nop 1
	v_writelane_b32 v200, s39, 27
	s_nop 1
	v_writelane_b32 v200, s40, 28
	s_nop 1
	v_writelane_b32 v200, s41, 29
	s_nop 1
	v_writelane_b32 v200, s42, 30
	s_nop 1
	v_writelane_b32 v200, s43, 31
	s_nop 1
	v_writelane_b32 v200, s44, 32
	s_nop 1
	v_writelane_b32 v200, s45, 33
	s_nop 1
	v_writelane_b32 v200, s46, 34
	s_nop 1
	v_writelane_b32 v200, s47, 35
	s_nop 1
	v_writelane_b32 v200, s48, 36
	s_nop 1
	v_writelane_b32 v200, s49, 37
	s_nop 1
	v_writelane_b32 v200, s50, 38
	s_nop 1
	v_writelane_b32 v200, s51, 39
	s_nop 1
	s_mov_b32 s99, 6
	s_mov_b32 s98, 2
	s_mov_b32 s101, 224
	s_add_i32 s100, s96, 1728
	s_branch .Ltc_next

.LBB0_1361:
	s_cmp_lt_u32 s96, 128
	s_cbranch_scc1 .Ltc_skip_7
	v_writelane_b32 v200, s0, 0
	s_nop 1
	v_writelane_b32 v200, s1, 1
	s_nop 1
	v_writelane_b32 v200, s2, 2
	s_nop 1
	v_writelane_b32 v200, s3, 3
	s_nop 1
	v_writelane_b32 v200, s4, 4
	s_nop 1
	v_writelane_b32 v200, s5, 5
	s_nop 1
	v_writelane_b32 v200, s6, 6
	s_nop 1
	v_writelane_b32 v200, s7, 7
	s_nop 1
	v_writelane_b32 v200, s10, 8
	s_nop 1
	v_writelane_b32 v200, s11, 9
	s_nop 1
	v_writelane_b32 v200, s12, 10
	s_nop 1
	v_writelane_b32 v200, s13, 11
	s_nop 1
	v_writelane_b32 v200, s14, 12
	s_nop 1
	v_writelane_b32 v200, s15, 13
	s_nop 1
	v_writelane_b32 v200, s16, 14
	s_nop 1
	v_writelane_b32 v200, s17, 15
	s_nop 1
	v_writelane_b32 v200, s18, 16
	s_nop 1
	v_writelane_b32 v200, s19, 17
	s_nop 1
	v_writelane_b32 v200, s20, 18
	s_nop 1
	v_writelane_b32 v200, s21, 19
	s_nop 1
	v_writelane_b32 v200, s22, 20
	s_nop 1
	v_writelane_b32 v200, s23, 21
	s_nop 1
	v_writelane_b32 v200, s24, 22
	s_nop 1
	v_writelane_b32 v200, s25, 23
	s_nop 1
	v_writelane_b32 v200, s36, 24
	s_nop 1
	v_writelane_b32 v200, s37, 25
	s_nop 1
	v_writelane_b32 v200, s38, 26
	s_nop 1
	v_writelane_b32 v200, s39, 27
	s_nop 1
	v_writelane_b32 v200, s40, 28
	s_nop 1
	v_writelane_b32 v200, s41, 29
	s_nop 1
	v_writelane_b32 v200, s42, 30
	s_nop 1
	v_writelane_b32 v200, s43, 31
	s_nop 1
	v_writelane_b32 v200, s44, 32
	s_nop 1
	v_writelane_b32 v200, s45, 33
	s_nop 1
	v_writelane_b32 v200, s46, 34
	s_nop 1
	v_writelane_b32 v200, s47, 35
	s_nop 1
	v_writelane_b32 v200, s48, 36
	s_nop 1
	v_writelane_b32 v200, s49, 37
	s_nop 1
	v_writelane_b32 v200, s50, 38
	s_nop 1
	v_writelane_b32 v200, s51, 39
	s_nop 1
	s_mov_b32 s99, 7
	s_mov_b32 s98, 2
	s_mov_b32 s101, 128
	s_add_i32 s100, s96, 2080
	s_branch .Ltc_s1_back

.LBB0_1495:
	s_cmp_lt_u32 s96, 48
	s_cbranch_scc1 .Ltc_skip_8
	v_writelane_b32 v200, s0, 0
	s_nop 1
	v_writelane_b32 v200, s1, 1
	s_nop 1
	v_writelane_b32 v200, s2, 2
	s_nop 1
	v_writelane_b32 v200, s3, 3
	s_nop 1
	v_writelane_b32 v200, s4, 4
	s_nop 1
	v_writelane_b32 v200, s5, 5
	s_nop 1
	v_writelane_b32 v200, s6, 6
	s_nop 1
	v_writelane_b32 v200, s7, 7
	s_nop 1
	v_writelane_b32 v200, s10, 8
	s_nop 1
	v_writelane_b32 v200, s11, 9
	s_nop 1
	v_writelane_b32 v200, s12, 10
	s_nop 1
	v_writelane_b32 v200, s13, 11
	s_nop 1
	v_writelane_b32 v200, s14, 12
	s_nop 1
	v_writelane_b32 v200, s15, 13
	s_nop 1
	v_writelane_b32 v200, s16, 14
	s_nop 1
	v_writelane_b32 v200, s17, 15
	s_nop 1
	v_writelane_b32 v200, s18, 16
	s_nop 1
	v_writelane_b32 v200, s19, 17
	s_nop 1
	v_writelane_b32 v200, s20, 18
	s_nop 1
	v_writelane_b32 v200, s21, 19
	s_nop 1
	v_writelane_b32 v200, s22, 20
	s_nop 1
	v_writelane_b32 v200, s23, 21
	s_nop 1
	v_writelane_b32 v200, s24, 22
	s_nop 1
	v_writelane_b32 v200, s25, 23
	s_nop 1
	v_writelane_b32 v200, s36, 24
	s_nop 1
	v_writelane_b32 v200, s37, 25
	s_nop 1
	v_writelane_b32 v200, s38, 26
	s_nop 1
	v_writelane_b32 v200, s39, 27
	s_nop 1
	v_writelane_b32 v200, s40, 28
	s_nop 1
	v_writelane_b32 v200, s41, 29
	s_nop 1
	v_writelane_b32 v200, s42, 30
	s_nop 1
	v_writelane_b32 v200, s43, 31
	s_nop 1
	v_writelane_b32 v200, s44, 32
	s_nop 1
	v_writelane_b32 v200, s45, 33
	s_nop 1
	v_writelane_b32 v200, s46, 34
	s_nop 1
	v_writelane_b32 v200, s47, 35
	s_nop 1
	v_writelane_b32 v200, s48, 36
	s_nop 1
	v_writelane_b32 v200, s49, 37
	s_nop 1
	v_writelane_b32 v200, s50, 38
	s_nop 1
	v_writelane_b32 v200, s51, 39
	s_nop 1
	s_mov_b32 s99, 8
	s_mov_b32 s98, 2
	s_mov_b32 s101, 208
	s_add_i32 s100, s96, 2416
	s_branch .Ltc_s1_back

.LBB0_1636:
	s_cmp_lt_u32 s96, 64
	s_cbranch_scc1 .Ltc_skip_9
	v_writelane_b32 v200, s0, 0
	s_nop 1
	v_writelane_b32 v200, s1, 1
	s_nop 1
	v_writelane_b32 v200, s2, 2
	s_nop 1
	v_writelane_b32 v200, s3, 3
	s_nop 1
	v_writelane_b32 v200, s4, 4
	s_nop 1
	v_writelane_b32 v200, s5, 5
	s_nop 1
	v_writelane_b32 v200, s6, 6
	s_nop 1
	v_writelane_b32 v200, s7, 7
	s_nop 1
	v_writelane_b32 v200, s10, 8
	s_nop 1
	v_writelane_b32 v200, s11, 9
	s_nop 1
	v_writelane_b32 v200, s12, 10
	s_nop 1
	v_writelane_b32 v200, s13, 11
	s_nop 1
	v_writelane_b32 v200, s14, 12
	s_nop 1
	v_writelane_b32 v200, s15, 13
	s_nop 1
	v_writelane_b32 v200, s16, 14
	s_nop 1
	v_writelane_b32 v200, s17, 15
	s_nop 1
	v_writelane_b32 v200, s18, 16
	s_nop 1
	v_writelane_b32 v200, s19, 17
	s_nop 1
	v_writelane_b32 v200, s20, 18
	s_nop 1
	v_writelane_b32 v200, s21, 19
	s_nop 1
	v_writelane_b32 v200, s22, 20
	s_nop 1
	v_writelane_b32 v200, s23, 21
	s_nop 1
	v_writelane_b32 v200, s24, 22
	s_nop 1
	v_writelane_b32 v200, s25, 23
	s_nop 1
	v_writelane_b32 v200, s36, 24
	s_nop 1
	v_writelane_b32 v200, s37, 25
	s_nop 1
	v_writelane_b32 v200, s38, 26
	s_nop 1
	v_writelane_b32 v200, s39, 27
	s_nop 1
	v_writelane_b32 v200, s40, 28
	s_nop 1
	v_writelane_b32 v200, s41, 29
	s_nop 1
	v_writelane_b32 v200, s42, 30
	s_nop 1
	v_writelane_b32 v200, s43, 31
	s_nop 1
	v_writelane_b32 v200, s44, 32
	s_nop 1
	v_writelane_b32 v200, s45, 33
	s_nop 1
	v_writelane_b32 v200, s46, 34
	s_nop 1
	v_writelane_b32 v200, s47, 35
	s_nop 1
	v_writelane_b32 v200, s48, 36
	s_nop 1
	v_writelane_b32 v200, s49, 37
	s_nop 1
	v_writelane_b32 v200, s50, 38
	s_nop 1
	v_writelane_b32 v200, s51, 39
	s_nop 1
	s_mov_b32 s99, 9
	s_mov_b32 s98, 1
	s_mov_b32 s101, 192
	s_add_i32 s100, s96, 2816
	s_branch .Ltc_s1_back

.LBB0_1711:
	s_cmp_lt_u32 s96, 32
	s_cbranch_scc1 .Ltc_skip_10
	v_writelane_b32 v200, s0, 0
	s_nop 1
	v_writelane_b32 v200, s1, 1
	s_nop 1
	v_writelane_b32 v200, s2, 2
	s_nop 1
	v_writelane_b32 v200, s3, 3
	s_nop 1
	v_writelane_b32 v200, s4, 4
	s_nop 1
	v_writelane_b32 v200, s5, 5
	s_nop 1
	v_writelane_b32 v200, s6, 6
	s_nop 1
	v_writelane_b32 v200, s7, 7
	s_nop 1
	v_writelane_b32 v200, s10, 8
	s_nop 1
	v_writelane_b32 v200, s11, 9
	s_nop 1
	v_writelane_b32 v200, s12, 10
	s_nop 1
	v_writelane_b32 v200, s13, 11
	s_nop 1
	v_writelane_b32 v200, s14, 12
	s_nop 1
	v_writelane_b32 v200, s15, 13
	s_nop 1
	v_writelane_b32 v200, s16, 14
	s_nop 1
	v_writelane_b32 v200, s17, 15
	s_nop 1
	v_writelane_b32 v200, s18, 16
	s_nop 1
	v_writelane_b32 v200, s19, 17
	s_nop 1
	v_writelane_b32 v200, s20, 18
	s_nop 1
	v_writelane_b32 v200, s21, 19
	s_nop 1
	v_writelane_b32 v200, s22, 20
	s_nop 1
	v_writelane_b32 v200, s23, 21
	s_nop 1
	v_writelane_b32 v200, s24, 22
	s_nop 1
	v_writelane_b32 v200, s25, 23
	s_nop 1
	v_writelane_b32 v200, s36, 24
	s_nop 1
	v_writelane_b32 v200, s37, 25
	s_nop 1
	v_writelane_b32 v200, s38, 26
	s_nop 1
	v_writelane_b32 v200, s39, 27
	s_nop 1
	v_writelane_b32 v200, s40, 28
	s_nop 1
	v_writelane_b32 v200, s41, 29
	s_nop 1
	v_writelane_b32 v200, s42, 30
	s_nop 1
	v_writelane_b32 v200, s43, 31
	s_nop 1
	v_writelane_b32 v200, s44, 32
	s_nop 1
	v_writelane_b32 v200, s45, 33
	s_nop 1
	v_writelane_b32 v200, s46, 34
	s_nop 1
	v_writelane_b32 v200, s47, 35
	s_nop 1
	v_writelane_b32 v200, s48, 36
	s_nop 1
	v_writelane_b32 v200, s49, 37
	s_nop 1
	v_writelane_b32 v200, s50, 38
	s_nop 1
	v_writelane_b32 v200, s51, 39
	s_nop 1
	s_mov_b32 s99, 10
	s_mov_b32 s98, 2
	s_mov_b32 s101, 224
	s_add_i32 s100, s96, 3040
	s_branch .Ltc_s1_back

.LBB0_2020:
	s_cmp_lt_u32 s96, 128
	s_cbranch_scc1 .Ltc_skip_11
	v_writelane_b32 v200, s0, 0
	s_nop 1
	v_writelane_b32 v200, s1, 1
	s_nop 1
	v_writelane_b32 v200, s2, 2
	s_nop 1
	v_writelane_b32 v200, s3, 3
	s_nop 1
	v_writelane_b32 v200, s4, 4
	s_nop 1
	v_writelane_b32 v200, s5, 5
	s_nop 1
	v_writelane_b32 v200, s6, 6
	s_nop 1
	v_writelane_b32 v200, s7, 7
	s_nop 1
	v_writelane_b32 v200, s10, 8
	s_nop 1
	v_writelane_b32 v200, s11, 9
	s_nop 1
	v_writelane_b32 v200, s12, 10
	s_nop 1
	v_writelane_b32 v200, s13, 11
	s_nop 1
	v_writelane_b32 v200, s14, 12
	s_nop 1
	v_writelane_b32 v200, s15, 13
	s_nop 1
	v_writelane_b32 v200, s16, 14
	s_nop 1
	v_writelane_b32 v200, s17, 15
	s_nop 1
	v_writelane_b32 v200, s18, 16
	s_nop 1
	v_writelane_b32 v200, s19, 17
	s_nop 1
	v_writelane_b32 v200, s20, 18
	s_nop 1
	v_writelane_b32 v200, s21, 19
	s_nop 1
	v_writelane_b32 v200, s22, 20
	s_nop 1
	v_writelane_b32 v200, s23, 21
	s_nop 1
	v_writelane_b32 v200, s24, 22
	s_nop 1
	v_writelane_b32 v200, s25, 23
	s_nop 1
	v_writelane_b32 v200, s36, 24
	s_nop 1
	v_writelane_b32 v200, s37, 25
	s_nop 1
	v_writelane_b32 v200, s38, 26
	s_nop 1
	v_writelane_b32 v200, s39, 27
	s_nop 1
	v_writelane_b32 v200, s40, 28
	s_nop 1
	v_writelane_b32 v200, s41, 29
	s_nop 1
	v_writelane_b32 v200, s42, 30
	s_nop 1
	v_writelane_b32 v200, s43, 31
	s_nop 1
	v_writelane_b32 v200, s44, 32
	s_nop 1
	v_writelane_b32 v200, s45, 33
	s_nop 1
	v_writelane_b32 v200, s46, 34
	s_nop 1
	v_writelane_b32 v200, s47, 35
	s_nop 1
	v_writelane_b32 v200, s48, 36
	s_nop 1
	v_writelane_b32 v200, s49, 37
	s_nop 1
	v_writelane_b32 v200, s50, 38
	s_nop 1
	v_writelane_b32 v200, s51, 39
	s_nop 1
	s_mov_b32 s99, 11
	s_mov_b32 s98, 2
	s_mov_b32 s101, 128
	s_add_i32 s100, s96, 3392
	s_branch .Ltc_s2_back

.LBB0_2154:
	s_cmp_lt_u32 s96, 32
	s_cbranch_scc1 .Ltc_skip_12
	v_writelane_b32 v200, s0, 0
	s_nop 1
	v_writelane_b32 v200, s1, 1
	s_nop 1
	v_writelane_b32 v200, s2, 2
	s_nop 1
	v_writelane_b32 v200, s3, 3
	s_nop 1
	v_writelane_b32 v200, s4, 4
	s_nop 1
	v_writelane_b32 v200, s5, 5
	s_nop 1
	v_writelane_b32 v200, s6, 6
	s_nop 1
	v_writelane_b32 v200, s7, 7
	s_nop 1
	v_writelane_b32 v200, s10, 8
	s_nop 1
	v_writelane_b32 v200, s11, 9
	s_nop 1
	v_writelane_b32 v200, s12, 10
	s_nop 1
	v_writelane_b32 v200, s13, 11
	s_nop 1
	v_writelane_b32 v200, s14, 12
	s_nop 1
	v_writelane_b32 v200, s15, 13
	s_nop 1
	v_writelane_b32 v200, s16, 14
	s_nop 1
	v_writelane_b32 v200, s17, 15
	s_nop 1
	v_writelane_b32 v200, s18, 16
	s_nop 1
	v_writelane_b32 v200, s19, 17
	s_nop 1
	v_writelane_b32 v200, s20, 18
	s_nop 1
	v_writelane_b32 v200, s21, 19
	s_nop 1
	v_writelane_b32 v200, s22, 20
	s_nop 1
	v_writelane_b32 v200, s23, 21
	s_nop 1
	v_writelane_b32 v200, s24, 22
	s_nop 1
	v_writelane_b32 v200, s25, 23
	s_nop 1
	v_writelane_b32 v200, s36, 24
	s_nop 1
	v_writelane_b32 v200, s37, 25
	s_nop 1
	v_writelane_b32 v200, s38, 26
	s_nop 1
	v_writelane_b32 v200, s39, 27
	s_nop 1
	v_writelane_b32 v200, s40, 28
	s_nop 1
	v_writelane_b32 v200, s41, 29
	s_nop 1
	v_writelane_b32 v200, s42, 30
	s_nop 1
	v_writelane_b32 v200, s43, 31
	s_nop 1
	v_writelane_b32 v200, s44, 32
	s_nop 1
	v_writelane_b32 v200, s45, 33
	s_nop 1
	v_writelane_b32 v200, s46, 34
	s_nop 1
	v_writelane_b32 v200, s47, 35
	s_nop 1
	v_writelane_b32 v200, s48, 36
	s_nop 1
	v_writelane_b32 v200, s49, 37
	s_nop 1
	v_writelane_b32 v200, s50, 38
	s_nop 1
	v_writelane_b32 v200, s51, 39
	s_nop 1
	s_mov_b32 s99, 12
	s_mov_b32 s98, 2
	s_mov_b32 s101, 224
	s_add_i32 s100, s96, 3744
	s_branch .Ltc_s2_back
